# stack14 plus back-edge rotation of the four attention loops: loop-back barrier is the loop head, exit test and slot rotation in front of it, exit path has its own wait and barrier
# baseline (speedup 1.0000x reference)
; DI int tid_fresh(int wave) { return wave * 64 + lane_fresh(); }
; DI void attn_pass(const Frame& F, CvRide& cv, const bf16_t* __restrict__ Qb, const bf16_t* __restrict__ Kh, const bf16_t* __restrict__ Vh, char* lds, f32x16 (&o)[4], float& l_out, const int wave_s) {
;     const int tid = tid_fresh(wave_s), wid = tid >> 6, lane = tid & 63, r32 = lane & 31, hi = lane >> 5;
;     char* V_lds = lds + OFF_V; char* K_lds = lds + OFF_K;
;     float m_ref = 0.f, l_reg = 0.f; bf16x8 qr[4]; f32x16 negm = f32x16{};
; #pragma unroll
;     for (int d = 0; d < 4; ++d) o[d] = f32x16{};
;     const bf16_t* Qw = Qb + (size_t)(wid * 32 + r32) * 64 + hi * 8;
; #pragma unroll
;     for (int d0 = 0; d0 < 4; ++d0) qr[d0] = *reinterpret_cast<const bf16x8*>(Qw + d0 * 16);
;     const int sr = tid >> 4, sc = (tid & 15) * 8, vst0 = v_st(sr, sc), vst1 = v_st(32 + sr, sc);
;     const int kr = tid >> 3, kcb = (tid & 7) * 16, kst = AT_KSWZ(kr, kcb);
;     const int vb0 = (int)(uintptr_t)V_lds + v_rd_base(lane);
;     struct { bf16x8 vs0, vs1, ks0; } sr_[1];
;     const unsigned gvo = (unsigned)((sr * 128 + sc) * 2), gko = (unsigned)((kr * 64 + (tid & 7) * 8) * 2);
;     ...
;     const unsigned cv_ldo = (unsigned)(((tid >> 4) * 2 * 2048 + (tid & 15) * 4) * 4), cv_sto = (unsigned)((tid >> 3) * 2048 + 8 * (tid & 7));
;     const int cv_lw = OFF_CV + (4 * (tid & 15)) * 68 + 2 * (tid >> 4), cv_lr = OFF_CV + (tid >> 3) * 68 + 8 * (tid & 7);
;     f32x4 cvA = f32x4{}, cvB = f32x4{}; unsigned cvr0 = 0, cvr1 = 0;
;     ...
;     f32x16 pA0, pA1, pB0, pB1; float alA, alB; bf16x8 pa0, pa1, pa2, pa3; constexpr int NT = S / 64;
;     constexpr int SE = 0;
;     {
;         bf16x8 v10 = *reinterpret_cast<const bf16x8*>(&Vh[(size_t)(64 + sr) * 128 + sc]), v11 = *reinterpret_cast<const bf16x8*>(&Vh[(size_t)(96 + sr) * 128 + sc]);
;         bf16x8 k10 = *reinterpret_cast<const bf16x8*>(&Kh[(size_t)(64 + kr) * 64 + (tid & 7) * 8]);
;         AT_SLOAD(SE, 0); asm volatile("s_waitcnt vmcnt(0)" ::: "memory");
;         __syncthreads();
;         AT_SWRITE(0, SE);
;         *(bf16x8*)(V_lds + SHM_V + vst0) = v10; *(bf16x8*)(V_lds + SHM_V + vst1) = v11; *(bf16x8*)(K_lds + SHM_K + kst) = k10;
;         __syncthreads();
;     }
;     qkt(pA0, pA1, K_lds, qr, negm, r32, hi); partialSM(pA0, pA1, m_ref, negm, alA);
;     int s_prev = 0, s_cur = 1, s_next = 2;
.LBB4_691:
	v_lshlrev_b32_e32 v24, 4, v21
	v_lshlrev_b32_e32 v23, 3, v21
	v_and_b32_e32 v24, 0xc0, v24
	v_lshlrev_b32_e32 v21, 1, v21
	v_and_or_b32 v24, v23, 24, v24
	v_and_b32_e32 v21, 32, v21
	v_and_b32_e32 v23, 0x100, v23
	s_cmp_lg_u32 0, -1
	v_or3_b32 v199, v24, v21, v23
	s_cselect_b32 s2, 0, 0
	v_add_u32_e32 v192, s2, v199
	s_movk_i32 s2, 0x44
	v_lshl_or_b32 v209, v16, 14, v18
	v_mul_lo_u32 v16, v20, s2
	v_exp_f32_e32 v216, v0
	v_exp_f32_e32 v218, v1
	v_exp_f32_e32 v179, v2
	v_exp_f32_e32 v217, v3
	v_exp_f32_e32 v177, v4
	v_exp_f32_e32 v215, v5
	v_exp_f32_e32 v176, v6
	v_exp_f32_e32 v178, v7
	v_exp_f32_e32 v173, v8
	v_exp_f32_e32 v175, v9
	v_exp_f32_e32 v171, v10
	v_exp_f32_e32 v174, v11
	v_exp_f32_e32 v169, v12
	v_exp_f32_e32 v172, v13
	v_exp_f32_e32 v168, v14
	v_exp_f32_e32 v170, v15
	v_add_u32_e32 v0, 0, v19
	s_mov_b32 s2, 0x22000
	v_mov_b32_e32 v182, 0
	v_add3_u32 v190, v0, v16, s2
	v_add_u32_e32 v0, 0, v22
	v_mov_b32_e32 v162, v182
	v_mov_b32_e32 v163, v182
	v_mov_b32_e32 v32, v182
	v_mov_b32_e32 v33, v182
	v_mov_b32_e32 v46, v182
	v_mov_b32_e32 v47, v182
	v_lshl_or_b32 v189, v20, 11, v19
	v_add3_u32 v191, v0, v17, s2
	v_mov_b32_e32 v183, v182
	v_mov_b32_e32 v160, v182
	v_mov_b32_e32 v161, v182
	v_mov_b32_e32 v34, v182
	v_mov_b32_e32 v35, v182
	v_mov_b32_e32 v36, v182
	v_mov_b32_e32 v37, v182
	v_mov_b32_e32 v38, v182
	v_mov_b32_e32 v39, v182
	v_mov_b32_e32 v40, v182
	v_mov_b32_e32 v41, v182
	v_mov_b32_e32 v42, v182
	v_mov_b32_e32 v43, v182
	v_mov_b32_e32 v44, v182
	v_mov_b32_e32 v45, v182
	v_mov_b64_e32 v[62:63], v[46:47]
	v_mov_b64_e32 v[16:17], v[32:33]
	v_mov_b64_e32 v[0:1], v[32:33]
	v_mov_b64_e32 v[166:167], v[162:163]
	s_mov_b32 s36, -1
	s_mul_i32 s59, s33, 6
	s_mov_b32 s64, 2
	s_mov_b64 s[12:13], 0
	s_mov_b32 s62, 0xc3e00000
	v_mov_b32_e32 v211, 0x43e00000
	s_mov_b64 s[28:29], s[16:17]
	s_mov_b64 s[30:31], s[18:19]
	s_mov_b32 s58, 0
	s_mov_b32 s26, 0
	s_mov_b64 s[10:11], 0
	s_mov_b64 s[8:9], 0
	v_mov_b64_e32 v[60:61], v[44:45]
	v_mov_b64_e32 v[58:59], v[42:43]
	v_mov_b64_e32 v[56:57], v[40:41]
	v_mov_b64_e32 v[54:55], v[38:39]
	v_mov_b64_e32 v[52:53], v[36:37]
	v_mov_b64_e32 v[50:51], v[34:35]
	v_mov_b64_e32 v[48:49], v[32:33]
	v_mov_b64_e32 v[18:19], v[34:35]
	v_mov_b64_e32 v[20:21], v[36:37]
	v_mov_b64_e32 v[22:23], v[38:39]
	v_mov_b64_e32 v[24:25], v[40:41]
	v_mov_b64_e32 v[26:27], v[42:43]
	v_mov_b64_e32 v[28:29], v[44:45]
	v_mov_b64_e32 v[30:31], v[46:47]
	v_mov_b64_e32 v[2:3], v[34:35]
	v_mov_b64_e32 v[4:5], v[36:37]
	v_mov_b64_e32 v[6:7], v[38:39]
	v_mov_b64_e32 v[8:9], v[40:41]
	v_mov_b64_e32 v[10:11], v[42:43]
	v_mov_b64_e32 v[12:13], v[44:45]
	v_mov_b64_e32 v[14:15], v[46:47]
	v_mov_b64_e32 v[164:165], v[160:161]
	s_mov_b32 s34, 0
	s_mov_b32 s65, 1
	v_mov_b64_e32 v[184:185], v[182:183]
	v_mov_b32_e32 v81, v80
	v_mov_b32_e32 v82, v80
	v_mov_b32_e32 v83, v80
	v_mov_b32_e32 v84, v80
	v_mov_b32_e32 v85, v80
	v_mov_b32_e32 v86, v80
	v_mov_b32_e32 v87, v80
	v_mov_b32_e32 v88, v80
	v_mov_b32_e32 v89, v80
	v_mov_b32_e32 v90, v80
	v_mov_b32_e32 v91, v80
	v_mov_b32_e32 v92, v80
	v_mov_b32_e32 v93, v80
	v_mov_b32_e32 v94, v80
	v_mov_b32_e32 v95, v80
	v_mov_b32_e32 v255, 0x3f600000
	s_mov_b32 s93, 0x3b000000
	v_mbcnt_lo_u32_b32 v253, -1, 0
	v_mbcnt_hi_u32_b32 v253, -1, v253
	v_lshrrev_b32_e32 v253, 5, v253
	v_mul_u32_u24_e32 v253, 0x700, v253
	v_add_u32_e32 v253, v253, v192
	s_nop 0
	s_branch .LBB4_692
.Lrot_h1:
	s_waitcnt lgkmcnt(0)
	s_barrier
.LBB4_692:
	s_lshl_b32 s92, s65, 13
	v_add_u32_e32 v68, s92, v204
	ds_read_b128 v[64:67], v68 offset:49152
	ds_read_b128 v[68:71], v68 offset:53248
	s_cmp_lg_u32 s26, 0
	s_mov_b32 s66, s65
	s_cselect_b64 s[2:3], -1, 0
	s_cmp_eq_u32 s26, 0
	s_mov_b32 s65, s34
	s_cbranch_scc1 .LBB4_694
	s_andn2_b32 s26, 1, s58
	s_mulk_i32 s26, 0x1100
	v_add_u32_e32 v252, s26, v190
	ds_read2_b32 v[184:185], v252 offset1:1

; DI void pv_all_sm(f32x16* o, int vb, bf16x8 pa0, bf16x8 pa1, bf16x8 pa2, bf16x8 pa3, f32x16& p0, f32x16& p1, float& m_ref, f32x16& negm, float& alpha) {
;     ...
;     for (int r = 0; r < 16; ++r) p0[r] = __builtin_amdgcn_exp2f(p0[r]);
; DI void attn_pass(const Frame& F, CvRide& cv, const bf16_t* __restrict__ Qb, const bf16_t* __restrict__ Kh, const bf16_t* __restrict__ Vh, char* lds, f32x16 (&o)[4], float& l_out, const int wave_s) {
;     ...
;     for (int j = 1; j + 2 < NT; j += 2) {
;         AT_STEP(pB0, pB1, pA0, pA1, alB, alA, j, true);
;         AT_STEP(pA0, pA1, pB0, pB1, alA, alB, j + 1, true);
;     }
.LBB4_733:
	s_add_u32 s30, s30, 0x4000
	v_exp_f32_e32 v216, v128
	v_exp_f32_e32 v218, v129
	v_exp_f32_e32 v179, v130
	v_exp_f32_e32 v217, v131
	v_exp_f32_e32 v177, v132
	v_exp_f32_e32 v215, v133
	v_exp_f32_e32 v176, v134
	v_exp_f32_e32 v178, v135
	v_exp_f32_e32 v173, v136
	v_exp_f32_e32 v175, v137
	v_exp_f32_e32 v171, v138
	v_exp_f32_e32 v174, v139
	v_exp_f32_e32 v169, v140
	v_exp_f32_e32 v172, v141
	v_exp_f32_e32 v168, v142
	v_exp_f32_e32 v170, v143
	s_addc_u32 s31, s31, 0
	s_add_u32 s28, s28, 0x8000
	v_fma_f32 v112, v210, v182, v183
	s_addc_u32 s29, s29, 0
	s_add_i32 s15, s15, 2
	v_fma_f32 v182, v112, v180, v213
	s_cmp_gt_u32 s15, 61
	s_cbranch_scc1 .Lrot_x1
	s_mov_b32 s34, s64
	s_mov_b32 s64, s66
	v_mov_b32_e32 v210, v186
	s_branch .Lrot_h1
.Lrot_x1:
	s_waitcnt lgkmcnt(0)
	s_barrier
	s_branch .LBB4_739
	s_nop 0

; DI int tid_fresh(int wave) { return wave * 64 + lane_fresh(); }
; DI void attn_pass(const Frame& F, CvRide& cv, const bf16_t* __restrict__ Qb, const bf16_t* __restrict__ Kh, const bf16_t* __restrict__ Vh, char* lds, f32x16 (&o)[4], float& l_out, const int wave_s) {
;     const int tid = tid_fresh(wave_s), wid = tid >> 6, lane = tid & 63, r32 = lane & 31, hi = lane >> 5;
;     char* V_lds = lds + OFF_V; char* K_lds = lds + OFF_K;
;     float m_ref = 0.f, l_reg = 0.f; bf16x8 qr[4]; f32x16 negm = f32x16{};
; #pragma unroll
;     for (int d = 0; d < 4; ++d) o[d] = f32x16{};
;     const bf16_t* Qw = Qb + (size_t)(wid * 32 + r32) * 64 + hi * 8;
; #pragma unroll
;     for (int d0 = 0; d0 < 4; ++d0) qr[d0] = *reinterpret_cast<const bf16x8*>(Qw + d0 * 16);
;     const int sr = tid >> 4, sc = (tid & 15) * 8, vst0 = v_st(sr, sc), vst1 = v_st(32 + sr, sc);
;     const int kr = tid >> 3, kcb = (tid & 7) * 16, kst = AT_KSWZ(kr, kcb);
;     const int vb0 = (int)(uintptr_t)V_lds + v_rd_base(lane);
;     struct { bf16x8 vs0, vs1, ks0; } sr_[1];
;     const unsigned gvo = (unsigned)((sr * 128 + sc) * 2), gko = (unsigned)((kr * 64 + (tid & 7) * 8) * 2);
;     ...
;     const unsigned cv_ldo = (unsigned)(((tid >> 4) * 2 * 2048 + (tid & 15) * 4) * 4), cv_sto = (unsigned)((tid >> 3) * 2048 + 8 * (tid & 7));
;     const int cv_lw = OFF_CV + (4 * (tid & 15)) * 68 + 2 * (tid >> 4), cv_lr = OFF_CV + (tid >> 3) * 68 + 8 * (tid & 7);
;     f32x4 cvA = f32x4{}, cvB = f32x4{}; unsigned cvr0 = 0, cvr1 = 0;
;     ...
;     f32x16 pA0, pA1, pB0, pB1; float alA, alB; bf16x8 pa0, pa1, pa2, pa3; constexpr int NT = S / 64;
;     constexpr int SE = 0;
;     {
;         bf16x8 v10 = *reinterpret_cast<const bf16x8*>(&Vh[(size_t)(64 + sr) * 128 + sc]), v11 = *reinterpret_cast<const bf16x8*>(&Vh[(size_t)(96 + sr) * 128 + sc]);
;         bf16x8 k10 = *reinterpret_cast<const bf16x8*>(&Kh[(size_t)(64 + kr) * 64 + (tid & 7) * 8]);
;         AT_SLOAD(SE, 0); asm volatile("s_waitcnt vmcnt(0)" ::: "memory");
;         __syncthreads();
;         AT_SWRITE(0, SE);
;         *(bf16x8*)(V_lds + SHM_V + vst0) = v10; *(bf16x8*)(V_lds + SHM_V + vst1) = v11; *(bf16x8*)(K_lds + SHM_K + kst) = k10;
;         __syncthreads();
;     }
;     qkt(pA0, pA1, K_lds, qr, negm, r32, hi); partialSM(pA0, pA1, m_ref, negm, alA);
;     int s_prev = 0, s_cur = 1, s_next = 2;
.LBB4_764:
	v_lshlrev_b32_e32 v24, 4, v22
	v_lshlrev_b32_e32 v23, 3, v22
	v_and_b32_e32 v24, 0xc0, v24
	v_lshlrev_b32_e32 v22, 1, v22
	v_and_or_b32 v24, v23, 24, v24
	v_and_b32_e32 v22, 32, v22
	v_and_b32_e32 v23, 0x100, v23
	s_cmp_lg_u32 0, -1
	v_or3_b32 v202, v24, v22, v23
	s_cselect_b32 s2, 0, 0
	v_add_u32_e32 v192, s2, v202
	s_movk_i32 s2, 0x44
	v_lshl_or_b32 v213, v16, 14, v18
	v_mul_lo_u32 v16, v20, s2
	v_exp_f32_e32 v220, v0
	v_exp_f32_e32 v222, v1
	v_exp_f32_e32 v179, v2
	v_exp_f32_e32 v221, v3
	v_exp_f32_e32 v177, v4
	v_exp_f32_e32 v219, v5
	v_exp_f32_e32 v176, v6
	v_exp_f32_e32 v178, v7
	v_exp_f32_e32 v173, v8
	v_exp_f32_e32 v175, v9
	v_exp_f32_e32 v171, v10
	v_exp_f32_e32 v174, v11
	v_exp_f32_e32 v169, v12
	v_exp_f32_e32 v172, v13
	v_exp_f32_e32 v168, v14
	v_exp_f32_e32 v170, v15
	v_add_u32_e32 v0, 0, v21
	s_mov_b32 s2, 0x22000
	v_add3_u32 v194, v0, v16, s2
	v_add_u32_e32 v0, 0, v19
	v_mov_b32_e32 v162, v183
	v_mov_b32_e32 v163, v183
	v_mov_b32_e32 v48, v183
	v_mov_b32_e32 v49, v183
	v_lshl_or_b32 v193, v20, 11, v21
	v_add3_u32 v195, v0, v17, s2
	v_mov_b32_e32 v182, v183
	v_mov_b32_e32 v160, v183
	v_mov_b32_e32 v161, v183
	v_mov_b32_e32 v50, v183
	v_mov_b32_e32 v51, v183
	v_mov_b32_e32 v52, v183
	v_mov_b32_e32 v53, v183
	v_mov_b32_e32 v54, v183
	v_mov_b32_e32 v55, v183
	v_mov_b32_e32 v56, v183
	v_mov_b32_e32 v57, v183
	v_mov_b32_e32 v58, v183
	v_mov_b32_e32 v59, v183
	v_mov_b32_e32 v60, v183
	v_mov_b32_e32 v61, v183
	v_mov_b32_e32 v62, v183
	v_mov_b32_e32 v63, v183
	v_mov_b64_e32 v[32:33], v[48:49]
	v_mov_b64_e32 v[16:17], v[48:49]
	v_mov_b64_e32 v[0:1], v[48:49]
	v_mov_b64_e32 v[166:167], v[162:163]
	s_mov_b32 s27, 1
	s_mov_b32 s28, 0xc3e00000
	v_mov_b32_e32 v214, 0x43e00000
	s_mov_b32 s20, 0
	v_mov_b64_e32 v[34:35], v[50:51]
	v_mov_b64_e32 v[36:37], v[52:53]
	v_mov_b64_e32 v[38:39], v[54:55]
	v_mov_b64_e32 v[40:41], v[56:57]
	v_mov_b64_e32 v[42:43], v[58:59]
	v_mov_b64_e32 v[44:45], v[60:61]
	v_mov_b64_e32 v[46:47], v[62:63]
	v_mov_b64_e32 v[18:19], v[50:51]
	v_mov_b64_e32 v[20:21], v[52:53]
	v_mov_b64_e32 v[22:23], v[54:55]
	v_mov_b64_e32 v[24:25], v[56:57]
	v_mov_b64_e32 v[26:27], v[58:59]
	v_mov_b64_e32 v[28:29], v[60:61]
	v_mov_b64_e32 v[30:31], v[62:63]
	v_mov_b64_e32 v[2:3], v[50:51]
	v_mov_b64_e32 v[4:5], v[52:53]
	v_mov_b64_e32 v[6:7], v[54:55]
	v_mov_b64_e32 v[8:9], v[56:57]
	v_mov_b64_e32 v[10:11], v[58:59]
	v_mov_b64_e32 v[12:13], v[60:61]
	v_mov_b64_e32 v[14:15], v[62:63]
	v_mov_b64_e32 v[164:165], v[160:161]
	s_mov_b32 s22, 0
	s_mov_b32 s29, 1
	v_mov_b64_e32 v[184:185], v[182:183]
	v_mov_b32_e32 v81, v80
	v_mov_b32_e32 v82, v80
	v_mov_b32_e32 v83, v80
	v_mov_b32_e32 v84, v80
	v_mov_b32_e32 v85, v80
	v_mov_b32_e32 v86, v80
	v_mov_b32_e32 v87, v80
	v_mov_b32_e32 v88, v80
	v_mov_b32_e32 v89, v80
	v_mov_b32_e32 v90, v80
	v_mov_b32_e32 v91, v80
	v_mov_b32_e32 v92, v80
	v_mov_b32_e32 v93, v80
	v_mov_b32_e32 v94, v80
	v_mov_b32_e32 v95, v80
	v_mov_b32_e32 v255, 0x3f600000
	s_mov_b32 s93, 0x3b000000
	v_mbcnt_lo_u32_b32 v253, -1, 0
	v_mbcnt_hi_u32_b32 v253, -1, v253
	v_lshrrev_b32_e32 v253, 5, v253
	v_mul_u32_u24_e32 v253, 0x700, v253
	v_add_u32_e32 v253, v253, v192
	s_nop 0
	s_branch .LBB4_765
.Lrot_h2:
	s_waitcnt lgkmcnt(0)
	s_barrier
.LBB4_765:
	s_lshl_b32 s92, s29, 13
	v_add_u32_e32 v68, s92, v207
	ds_read_b128 v[64:67], v68 offset:49152
	ds_read_b128 v[68:71], v68 offset:53248
	s_cmp_lg_u32 s20, 0
	s_mov_b32 s30, s29
	s_cselect_b64 s[2:3], -1, 0
	s_cmp_eq_u32 s20, 0
	s_mov_b32 s29, s22
	s_cbranch_scc1 .LBB4_767
	s_andn2_b32 s20, 1, s58
	s_mulk_i32 s20, 0x1100
	v_add_u32_e32 v252, s20, v194
	ds_read2_b32 v[184:185], v252 offset1:1

; DI void pv_all_sm(f32x16* o, int vb, bf16x8 pa0, bf16x8 pa1, bf16x8 pa2, bf16x8 pa3, f32x16& p0, f32x16& p1, float& m_ref, f32x16& negm, float& alpha) {
;     ...
; #pragma unroll
;     for (int r = 0; r < 16; ++r) p0[r] = __builtin_amdgcn_exp2f(p0[r]);
; DI void attn_pass(const Frame& F, CvRide& cv, const bf16_t* __restrict__ Qb, const bf16_t* __restrict__ Kh, const bf16_t* __restrict__ Vh, char* lds, f32x16 (&o)[4], float& l_out, const int wave_s) {
;     ...
;     for (int j = 1; j + 2 < NT; j += 2) {
;         AT_STEP(pB0, pB1, pA0, pA1, alB, alA, j, true);
;         AT_STEP(pA0, pA1, pB0, pB1, alA, alB, j + 1, true);
;     }
.LBB4_806:
	s_add_u32 s18, s18, 0x4000
	v_exp_f32_e32 v220, v128
	v_exp_f32_e32 v222, v129
	v_exp_f32_e32 v179, v130
	v_exp_f32_e32 v221, v131
	v_exp_f32_e32 v177, v132
	v_exp_f32_e32 v219, v133
	v_exp_f32_e32 v176, v134
	v_exp_f32_e32 v178, v135
	v_exp_f32_e32 v173, v136
	v_exp_f32_e32 v175, v137
	v_exp_f32_e32 v171, v138
	v_exp_f32_e32 v174, v139
	v_exp_f32_e32 v169, v140
	v_exp_f32_e32 v172, v141
	v_exp_f32_e32 v168, v142
	v_exp_f32_e32 v170, v143
	s_addc_u32 s19, s19, 0
	s_add_u32 s16, s16, 0x8000
	v_fma_f32 v112, v211, v183, v215
	s_addc_u32 s17, s17, 0
	s_add_i32 s27, s27, 2
	v_fma_f32 v183, v112, v180, v217
	s_cmp_gt_u32 s27, 61
	s_cbranch_scc1 .Lrot_x2
	s_mov_b32 s22, s15
	s_mov_b32 s15, s30
	v_mov_b32_e32 v211, v182
	s_branch .Lrot_h2

; DI int tid_fresh(int wave) { return wave * 64 + lane_fresh(); }
; DI void attn_pass(const Frame& F, CvRide& cv, const bf16_t* __restrict__ Qb, const bf16_t* __restrict__ Kh, const bf16_t* __restrict__ Vh, char* lds, f32x16 (&o)[4], float& l_out, const int wave_s) {
;     const int tid = tid_fresh(wave_s), wid = tid >> 6, lane = tid & 63, r32 = lane & 31, hi = lane >> 5;
;     char* V_lds = lds + OFF_V; char* K_lds = lds + OFF_K;
;     float m_ref = 0.f, l_reg = 0.f; bf16x8 qr[4]; f32x16 negm = f32x16{};
; #pragma unroll
;     for (int d = 0; d < 4; ++d) o[d] = f32x16{};
;     const bf16_t* Qw = Qb + (size_t)(wid * 32 + r32) * 64 + hi * 8;
; #pragma unroll
;     for (int d0 = 0; d0 < 4; ++d0) qr[d0] = *reinterpret_cast<const bf16x8*>(Qw + d0 * 16);
;     const int sr = tid >> 4, sc = (tid & 15) * 8, vst0 = v_st(sr, sc), vst1 = v_st(32 + sr, sc);
;     const int kr = tid >> 3, kcb = (tid & 7) * 16, kst = AT_KSWZ(kr, kcb);
;     const int vb0 = (int)(uintptr_t)V_lds + v_rd_base(lane);
;     struct { bf16x8 vs0, vs1, ks0; } sr_[1];
;     const unsigned gvo = (unsigned)((sr * 128 + sc) * 2), gko = (unsigned)((kr * 64 + (tid & 7) * 8) * 2);
;     ...
;     const unsigned cv_ldo = (unsigned)(((tid >> 4) * 2 * 2048 + (tid & 15) * 4) * 4), cv_sto = (unsigned)((tid >> 3) * 2048 + 8 * (tid & 7));
;     const int cv_lw = OFF_CV + (4 * (tid & 15)) * 68 + 2 * (tid >> 4), cv_lr = OFF_CV + (tid >> 3) * 68 + 8 * (tid & 7);
;     f32x4 cvA = f32x4{}, cvB = f32x4{}; unsigned cvr0 = 0, cvr1 = 0;
;     ...
;     f32x16 pA0, pA1, pB0, pB1; float alA, alB; bf16x8 pa0, pa1, pa2, pa3; constexpr int NT = S / 64;
;     constexpr int SE = 0;
;     {
;         bf16x8 v10 = *reinterpret_cast<const bf16x8*>(&Vh[(size_t)(64 + sr) * 128 + sc]), v11 = *reinterpret_cast<const bf16x8*>(&Vh[(size_t)(96 + sr) * 128 + sc]);
;         bf16x8 k10 = *reinterpret_cast<const bf16x8*>(&Kh[(size_t)(64 + kr) * 64 + (tid & 7) * 8]);
;         AT_SLOAD(SE, 0); asm volatile("s_waitcnt vmcnt(0)" ::: "memory");
;         __syncthreads();
;         AT_SWRITE(0, SE);
;         *(bf16x8*)(V_lds + SHM_V + vst0) = v10; *(bf16x8*)(V_lds + SHM_V + vst1) = v11; *(bf16x8*)(K_lds + SHM_K + kst) = k10;
;         __syncthreads();
;     }
;     qkt(pA0, pA1, K_lds, qr, negm, r32, hi); partialSM(pA0, pA1, m_ref, negm, alA);
;     int s_prev = 0, s_cur = 1, s_next = 2;
.LBB4_838:
	v_lshlrev_b32_e32 v24, 4, v22
	v_lshlrev_b32_e32 v23, 3, v22
	v_and_b32_e32 v24, 0xc0, v24
	v_lshlrev_b32_e32 v22, 1, v22
	v_and_or_b32 v24, v23, 24, v24
	v_and_b32_e32 v22, 32, v22
	v_and_b32_e32 v23, 0x100, v23
	s_cmp_lg_u32 0, -1
	v_or3_b32 v198, v24, v22, v23
	s_cselect_b32 s2, 0, 0
	v_add_u32_e32 v191, s2, v198
	s_movk_i32 s2, 0x44
	v_lshl_or_b32 v209, v16, 14, v18
	v_mul_lo_u32 v16, v20, s2
	v_exp_f32_e32 v216, v0
	v_exp_f32_e32 v218, v1
	v_exp_f32_e32 v179, v2
	v_exp_f32_e32 v217, v3
	v_exp_f32_e32 v177, v4
	v_exp_f32_e32 v215, v5
	v_exp_f32_e32 v176, v6
	v_exp_f32_e32 v178, v7
	v_exp_f32_e32 v173, v8
	v_exp_f32_e32 v175, v9
	v_exp_f32_e32 v171, v10
	v_exp_f32_e32 v174, v11
	v_exp_f32_e32 v169, v12
	v_exp_f32_e32 v172, v13
	v_exp_f32_e32 v168, v14
	v_exp_f32_e32 v170, v15
	v_add_u32_e32 v0, 0, v21
	s_mov_b32 s2, 0x22000
	v_add3_u32 v189, v0, v16, s2
	v_add_u32_e32 v0, 0, v19
	v_mov_b32_e32 v162, v183
	v_mov_b32_e32 v163, v183
	v_mov_b32_e32 v32, v183
	v_mov_b32_e32 v33, v183
	v_mov_b32_e32 v46, v183
	v_mov_b32_e32 v47, v183
	v_lshl_or_b32 v188, v20, 11, v21
	v_add3_u32 v190, v0, v17, s2
	v_mov_b32_e32 v182, v183
	v_mov_b32_e32 v160, v183
	v_mov_b32_e32 v161, v183
	v_mov_b32_e32 v34, v183
	v_mov_b32_e32 v35, v183
	v_mov_b32_e32 v36, v183
	v_mov_b32_e32 v37, v183
	v_mov_b32_e32 v38, v183
	v_mov_b32_e32 v39, v183
	v_mov_b32_e32 v40, v183
	v_mov_b32_e32 v41, v183
	v_mov_b32_e32 v42, v183
	v_mov_b32_e32 v43, v183
	v_mov_b32_e32 v44, v183
	v_mov_b32_e32 v45, v183
	v_mov_b64_e32 v[62:63], v[46:47]
	v_mov_b64_e32 v[16:17], v[32:33]
	v_mov_b64_e32 v[0:1], v[32:33]
	v_mov_b64_e32 v[166:167], v[162:163]
	s_mov_b32 s23, 1
	s_mov_b32 s57, 2
	s_mov_b32 s56, 0xc3e00000
	v_mov_b32_e32 v210, 0x43e00000
	s_mov_b64 s[28:29], s[16:17]
	s_mov_b32 s26, 0
	v_mov_b64_e32 v[60:61], v[44:45]
	v_mov_b64_e32 v[58:59], v[42:43]
	v_mov_b64_e32 v[56:57], v[40:41]
	v_mov_b64_e32 v[54:55], v[38:39]
	v_mov_b64_e32 v[52:53], v[36:37]
	v_mov_b64_e32 v[50:51], v[34:35]
	v_mov_b64_e32 v[48:49], v[32:33]
	v_mov_b64_e32 v[18:19], v[34:35]
	v_mov_b64_e32 v[20:21], v[36:37]
	v_mov_b64_e32 v[22:23], v[38:39]
	v_mov_b64_e32 v[24:25], v[40:41]
	v_mov_b64_e32 v[26:27], v[42:43]
	v_mov_b64_e32 v[28:29], v[44:45]
	v_mov_b64_e32 v[30:31], v[46:47]
	v_mov_b64_e32 v[2:3], v[34:35]
	v_mov_b64_e32 v[4:5], v[36:37]
	v_mov_b64_e32 v[6:7], v[38:39]
	v_mov_b64_e32 v[8:9], v[40:41]
	v_mov_b64_e32 v[10:11], v[42:43]
	v_mov_b64_e32 v[12:13], v[44:45]
	v_mov_b64_e32 v[14:15], v[46:47]
	v_mov_b64_e32 v[164:165], v[160:161]
	s_mov_b32 s30, 0
	s_mov_b32 s63, 1
	v_mov_b64_e32 v[184:185], v[182:183]
	v_mov_b32_e32 v81, v80
	v_mov_b32_e32 v82, v80
	v_mov_b32_e32 v83, v80
	v_mov_b32_e32 v84, v80
	v_mov_b32_e32 v85, v80
	v_mov_b32_e32 v86, v80
	v_mov_b32_e32 v87, v80
	v_mov_b32_e32 v88, v80
	v_mov_b32_e32 v89, v80
	v_mov_b32_e32 v90, v80
	v_mov_b32_e32 v91, v80
	v_mov_b32_e32 v92, v80
	v_mov_b32_e32 v93, v80
	v_mov_b32_e32 v94, v80
	v_mov_b32_e32 v95, v80
	v_mov_b32_e32 v255, 0x3f600000
	s_mov_b32 s93, 0x3b000000
	v_mbcnt_lo_u32_b32 v253, -1, 0
	v_mbcnt_hi_u32_b32 v253, -1, v253
	v_lshrrev_b32_e32 v253, 5, v253
	v_mul_u32_u24_e32 v253, 0x700, v253
	v_add_u32_e32 v253, v253, v191
	s_nop 0
	s_branch .LBB4_839
.Lrot_h3:
	s_waitcnt lgkmcnt(0)
	s_barrier
.LBB4_839:
	s_lshl_b32 s92, s63, 13
	v_add_u32_e32 v68, s92, v203
	ds_read_b128 v[64:67], v68 offset:49152
	ds_read_b128 v[68:71], v68 offset:53248
	s_cmp_lg_u32 s26, 0
	s_mov_b32 s64, s63
	s_cselect_b64 s[2:3], -1, 0
	s_cmp_eq_u32 s26, 0
	s_mov_b32 s63, s30
	s_cbranch_scc1 .LBB4_841
	s_andn2_b32 s26, 1, s58
	s_mulk_i32 s26, 0x1100
	v_add_u32_e32 v252, s26, v189
	ds_read2_b32 v[184:185], v252 offset1:1

; DI void pv_all_sm(f32x16* o, int vb, bf16x8 pa0, bf16x8 pa1, bf16x8 pa2, bf16x8 pa3, f32x16& p0, f32x16& p1, float& m_ref, f32x16& negm, float& alpha) {
;     ...
; #pragma unroll
;     for (int r = 0; r < 16; ++r) p0[r] = __builtin_amdgcn_exp2f(p0[r]);
; DI void attn_pass(const Frame& F, CvRide& cv, const bf16_t* __restrict__ Qb, const bf16_t* __restrict__ Kh, const bf16_t* __restrict__ Vh, char* lds, f32x16 (&o)[4], float& l_out, const int wave_s) {
;     ...
;     for (int j = 1; j + 2 < NT; j += 2) {
;         AT_STEP(pB0, pB1, pA0, pA1, alB, alA, j, true);
;         AT_STEP(pA0, pA1, pB0, pB1, alA, alB, j + 1, true);
;     }
.LBB4_880:
	s_add_u32 s24, s24, 0x4000
	v_exp_f32_e32 v216, v128
	v_exp_f32_e32 v218, v129
	v_exp_f32_e32 v179, v130
	v_exp_f32_e32 v217, v131
	v_exp_f32_e32 v177, v132
	v_exp_f32_e32 v215, v133
	v_exp_f32_e32 v176, v134
	v_exp_f32_e32 v178, v135
	v_exp_f32_e32 v173, v136
	v_exp_f32_e32 v175, v137
	v_exp_f32_e32 v171, v138
	v_exp_f32_e32 v174, v139
	v_exp_f32_e32 v169, v140
	v_exp_f32_e32 v172, v141
	v_exp_f32_e32 v168, v142
	v_exp_f32_e32 v170, v143
	s_addc_u32 s25, s25, 0
	s_add_u32 s28, s28, 0x8000
	v_fma_f32 v112, v207, v183, v211
	s_addc_u32 s29, s29, 0
	s_add_i32 s23, s23, 2
	v_fma_f32 v183, v112, v180, v213
	s_cmp_gt_u32 s23, 61
	s_cbranch_scc1 .Lrot_x3
	s_mov_b32 s30, s57
	s_mov_b32 s57, s64
	v_mov_b32_e32 v207, v182
	s_branch .Lrot_h3

; DI int tid_fresh(int wave) { return wave * 64 + lane_fresh(); }
; DI void attn_pass(const Frame& F, CvRide& cv, const bf16_t* __restrict__ Qb, const bf16_t* __restrict__ Kh, const bf16_t* __restrict__ Vh, char* lds, f32x16 (&o)[4], float& l_out, const int wave_s) {
;     const int tid = tid_fresh(wave_s), wid = tid >> 6, lane = tid & 63, r32 = lane & 31, hi = lane >> 5;
;     char* V_lds = lds + OFF_V; char* K_lds = lds + OFF_K;
;     float m_ref = 0.f, l_reg = 0.f; bf16x8 qr[4]; f32x16 negm = f32x16{};
; #pragma unroll
;     for (int d = 0; d < 4; ++d) o[d] = f32x16{};
;     const bf16_t* Qw = Qb + (size_t)(wid * 32 + r32) * 64 + hi * 8;
; #pragma unroll
;     for (int d0 = 0; d0 < 4; ++d0) qr[d0] = *reinterpret_cast<const bf16x8*>(Qw + d0 * 16);
;     const int sr = tid >> 4, sc = (tid & 15) * 8, vst0 = v_st(sr, sc), vst1 = v_st(32 + sr, sc);
;     const int kr = tid >> 3, kcb = (tid & 7) * 16, kst = AT_KSWZ(kr, kcb);
;     const int vb0 = (int)(uintptr_t)V_lds + v_rd_base(lane);
;     struct { bf16x8 vs0, vs1, ks0; } sr_[1];
;     const unsigned gvo = (unsigned)((sr * 128 + sc) * 2), gko = (unsigned)((kr * 64 + (tid & 7) * 8) * 2);
;     ...
;     const unsigned cv_ldo = (unsigned)(((tid >> 4) * 2 * 2048 + (tid & 15) * 4) * 4), cv_sto = (unsigned)((tid >> 3) * 2048 + 8 * (tid & 7));
;     const int cv_lw = OFF_CV + (4 * (tid & 15)) * 68 + 2 * (tid >> 4), cv_lr = OFF_CV + (tid >> 3) * 68 + 8 * (tid & 7);
;     f32x4 cvA = f32x4{}, cvB = f32x4{}; unsigned cvr0 = 0, cvr1 = 0;
;     ...
;     f32x16 pA0, pA1, pB0, pB1; float alA, alB; bf16x8 pa0, pa1, pa2, pa3; constexpr int NT = S / 64;
;     constexpr int SE = 0;
;     {
;         bf16x8 v10 = *reinterpret_cast<const bf16x8*>(&Vh[(size_t)(64 + sr) * 128 + sc]), v11 = *reinterpret_cast<const bf16x8*>(&Vh[(size_t)(96 + sr) * 128 + sc]);
;         bf16x8 k10 = *reinterpret_cast<const bf16x8*>(&Kh[(size_t)(64 + kr) * 64 + (tid & 7) * 8]);
;         AT_SLOAD(SE, 0); asm volatile("s_waitcnt vmcnt(0)" ::: "memory");
;         __syncthreads();
;         AT_SWRITE(0, SE);
;         *(bf16x8*)(V_lds + SHM_V + vst0) = v10; *(bf16x8*)(V_lds + SHM_V + vst1) = v11; *(bf16x8*)(K_lds + SHM_K + kst) = k10;
;         __syncthreads();
;     }
;     qkt(pA0, pA1, K_lds, qr, negm, r32, hi); partialSM(pA0, pA1, m_ref, negm, alA);
;     int s_prev = 0, s_cur = 1, s_next = 2;
.LBB4_912:
	v_lshlrev_b32_e32 v24, 4, v22
	v_lshlrev_b32_e32 v23, 3, v22
	v_and_b32_e32 v24, 0xc0, v24
	v_lshlrev_b32_e32 v22, 1, v22
	v_and_or_b32 v24, v23, 24, v24
	v_and_b32_e32 v22, 32, v22
	v_and_b32_e32 v23, 0x100, v23
	s_cmp_lg_u32 0, -1
	v_or3_b32 v202, v24, v22, v23
	s_cselect_b32 s2, 0, 0
	v_add_u32_e32 v192, s2, v202
	s_movk_i32 s2, 0x44
	v_lshl_or_b32 v213, v16, 14, v18
	v_mul_lo_u32 v16, v20, s2
	v_exp_f32_e32 v220, v0
	v_add_u32_e32 v0, 0, v21
	s_mov_b32 s2, 0x22000
	v_add3_u32 v194, v0, v16, s2
	v_add_u32_e32 v0, 0, v19
	v_add3_u32 v195, v0, v17, s2
	s_and_b32 s2, s33, 7
	s_lshl_b32 s2, s2, 2
	s_lshl_b32 s3, s60, 1
	v_exp_f32_e32 v222, v1
	v_exp_f32_e32 v179, v2
	v_exp_f32_e32 v221, v3
	v_exp_f32_e32 v177, v4
	v_exp_f32_e32 v219, v5
	v_exp_f32_e32 v176, v6
	v_exp_f32_e32 v178, v7
	v_exp_f32_e32 v173, v8
	v_exp_f32_e32 v175, v9
	v_exp_f32_e32 v171, v10
	v_exp_f32_e32 v174, v11
	v_exp_f32_e32 v169, v12
	v_exp_f32_e32 v172, v13
	v_exp_f32_e32 v168, v14
	v_exp_f32_e32 v170, v15
	s_add_i32 s2, s2, s3
	s_add_i32 s2, s2, 32
	v_mov_b32_e32 v162, v183
	v_mov_b32_e32 v163, v183
	v_mov_b32_e32 v48, v183
	v_mov_b32_e32 v49, v183
	v_lshl_or_b32 v193, v20, 11, v21
	s_ashr_i32 s3, s2, 31
	v_mov_b32_e32 v182, v183
	v_mov_b32_e32 v160, v183
	v_mov_b32_e32 v161, v183
	v_mov_b32_e32 v50, v183
	v_mov_b32_e32 v51, v183
	v_mov_b32_e32 v52, v183
	v_mov_b32_e32 v53, v183
	v_mov_b32_e32 v54, v183
	v_mov_b32_e32 v55, v183
	v_mov_b32_e32 v56, v183
	v_mov_b32_e32 v57, v183
	v_mov_b32_e32 v58, v183
	v_mov_b32_e32 v59, v183
	v_mov_b32_e32 v60, v183
	v_mov_b32_e32 v61, v183
	v_mov_b32_e32 v62, v183
	v_mov_b32_e32 v63, v183
	v_mov_b64_e32 v[32:33], v[48:49]
	v_mov_b64_e32 v[16:17], v[48:49]
	v_mov_b64_e32 v[0:1], v[48:49]
	v_mov_b64_e32 v[166:167], v[162:163]
	s_mov_b32 s27, 1
	s_lshl_b64 s[20:21], s[2:3], 19
	s_mov_b32 s28, 0xc3e00000
	v_mov_b32_e32 v214, 0x43e00000
	s_mov_b32 s18, 0
	v_mov_b64_e32 v[34:35], v[50:51]
	v_mov_b64_e32 v[36:37], v[52:53]
	v_mov_b64_e32 v[38:39], v[54:55]
	v_mov_b64_e32 v[40:41], v[56:57]
	v_mov_b64_e32 v[42:43], v[58:59]
	v_mov_b64_e32 v[44:45], v[60:61]
	v_mov_b64_e32 v[46:47], v[62:63]
	v_mov_b64_e32 v[18:19], v[50:51]
	v_mov_b64_e32 v[20:21], v[52:53]
	v_mov_b64_e32 v[22:23], v[54:55]
	v_mov_b64_e32 v[24:25], v[56:57]
	v_mov_b64_e32 v[26:27], v[58:59]
	v_mov_b64_e32 v[28:29], v[60:61]
	v_mov_b64_e32 v[30:31], v[62:63]
	v_mov_b64_e32 v[2:3], v[50:51]
	v_mov_b64_e32 v[4:5], v[52:53]
	v_mov_b64_e32 v[6:7], v[54:55]
	v_mov_b64_e32 v[8:9], v[56:57]
	v_mov_b64_e32 v[10:11], v[58:59]
	v_mov_b64_e32 v[12:13], v[60:61]
	v_mov_b64_e32 v[14:15], v[62:63]
	v_mov_b64_e32 v[164:165], v[160:161]
	s_mov_b32 s22, 0
	s_mov_b32 s29, 1
	v_mov_b64_e32 v[184:185], v[182:183]
	v_mov_b32_e32 v81, v80
	v_mov_b32_e32 v82, v80
	v_mov_b32_e32 v83, v80
	v_mov_b32_e32 v84, v80
	v_mov_b32_e32 v85, v80
	v_mov_b32_e32 v86, v80
	v_mov_b32_e32 v87, v80
	v_mov_b32_e32 v88, v80
	v_mov_b32_e32 v89, v80
	v_mov_b32_e32 v90, v80
	v_mov_b32_e32 v91, v80
	v_mov_b32_e32 v92, v80
	v_mov_b32_e32 v93, v80
	v_mov_b32_e32 v94, v80
	v_mov_b32_e32 v95, v80
	v_mov_b32_e32 v255, 0x3f600000
	s_mov_b32 s93, 0x3b000000
	v_mbcnt_lo_u32_b32 v253, -1, 0
	v_mbcnt_hi_u32_b32 v253, -1, v253
	v_lshrrev_b32_e32 v253, 5, v253
	v_mul_u32_u24_e32 v253, 0x700, v253
	v_add_u32_e32 v253, v253, v192
	s_nop 0
	s_branch .LBB4_913
.Lrot_h4:
	s_waitcnt lgkmcnt(0)
	s_barrier
.LBB4_913:
	s_lshl_b32 s92, s29, 13
	v_add_u32_e32 v68, s92, v207
	ds_read_b128 v[64:67], v68 offset:49152
	ds_read_b128 v[68:71], v68 offset:53248
	s_cmp_lg_u32 s18, 0
	s_mov_b32 s30, s29
	s_cselect_b64 s[2:3], -1, 0
	s_cmp_eq_u32 s18, 0
	s_mov_b32 s29, s22
	s_cbranch_scc1 .LBB4_915
	s_andn2_b32 s18, 1, s58
	s_mulk_i32 s18, 0x1100
	v_add_u32_e32 v252, s18, v194
	ds_read2_b32 v[184:185], v252 offset1:1

; DI void pv_all_sm(f32x16* o, int vb, bf16x8 pa0, bf16x8 pa1, bf16x8 pa2, bf16x8 pa3, f32x16& p0, f32x16& p1, float& m_ref, f32x16& negm, float& alpha) {
;     ...
; #pragma unroll
;     for (int r = 0; r < 16; ++r) p0[r] = __builtin_amdgcn_exp2f(p0[r]);
; DI void attn_pass(const Frame& F, CvRide& cv, const bf16_t* __restrict__ Qb, const bf16_t* __restrict__ Kh, const bf16_t* __restrict__ Vh, char* lds, f32x16 (&o)[4], float& l_out, const int wave_s) {
;     ...
;     for (int j = 1; j + 2 < NT; j += 2) {
;         AT_STEP(pB0, pB1, pA0, pA1, alB, alA, j, true);
;         AT_STEP(pA0, pA1, pB0, pB1, alA, alB, j + 1, true);
;     }
.LBB4_954:
	s_add_u32 s20, s20, 0x4000
	v_exp_f32_e32 v220, v128
	v_exp_f32_e32 v222, v129
	v_exp_f32_e32 v179, v130
	v_exp_f32_e32 v221, v131
	v_exp_f32_e32 v177, v132
	v_exp_f32_e32 v219, v133
	v_exp_f32_e32 v176, v134
	v_exp_f32_e32 v178, v135
	v_exp_f32_e32 v173, v136
	v_exp_f32_e32 v175, v137
	v_exp_f32_e32 v171, v138
	v_exp_f32_e32 v174, v139
	v_exp_f32_e32 v169, v140
	v_exp_f32_e32 v172, v141
	v_exp_f32_e32 v168, v142
	v_exp_f32_e32 v170, v143
	s_addc_u32 s21, s21, 0
	s_add_u32 s16, s16, 0x8000
	v_fma_f32 v112, v211, v183, v215
	s_addc_u32 s17, s17, 0
	s_add_i32 s27, s27, 2
	v_fma_f32 v183, v112, v180, v217
	s_cmp_gt_u32 s27, 61
	s_cbranch_scc1 .Lrot_x4
	s_mov_b32 s22, s15
	s_mov_b32 s15, s30
	v_mov_b32_e32 v211, v182
	s_branch .Lrot_h4
